# P9 accumulator init: 64 v_mov_b64 from the scaled-bias tuple (128 v_mov_b32 before)
# speedup vs baseline: 1.0127x; 1.0001x over previous
.LBB0_1006:
	s_ashr_i32 s3, s19, 31
	s_mov_b32 s2, s19
	s_lshl_b64 s[2:3], s[2:3], 19
	s_add_u32 s20, s17, s2
	s_addc_u32 s21, s30, s3
	s_and_b64 s[2:3], s[26:27], exec
	s_cselect_b32 s2, s21, s25
	s_cselect_b32 s3, s20, s24
	v_mov_b32_e32 v181, v169
	v_mov_b32_e32 v179, v169
	v_mov_b32_e32 v177, v169
	v_mov_b32_e32 v183, v169
	s_add_u32 s50, s24, 0x100
	s_addc_u32 s51, s25, 0
	v_lshl_add_u64 v[184:185], s[14:15], 0, v[182:183]
	v_lshl_add_u64 v[186:187], s[14:15], 0, v[176:177]
	v_lshl_add_u64 v[188:189], s[14:15], 0, v[178:179]
	v_lshl_add_u64 v[190:191], s[14:15], 0, v[180:181]
	s_mov_b32 s52, -2
	s_mov_b64 s[28:29], 0
	v_mov_b64_e32 v[34:35], v[212:213]
	v_mov_b64_e32 v[36:37], v[214:215]
	v_mov_b64_e32 v[38:39], v[208:209]
	v_mov_b64_e32 v[40:41], v[210:211]
	v_mov_b64_e32 v[42:43], v[220:221]
	v_mov_b64_e32 v[44:45], v[222:223]
	v_mov_b64_e32 v[46:47], v[216:217]
	v_mov_b64_e32 v[48:49], v[218:219]
	v_mov_b64_e32 v[50:51], v[212:213]
	v_mov_b64_e32 v[52:53], v[214:215]
	v_mov_b64_e32 v[54:55], v[220:221]
	v_mov_b64_e32 v[56:57], v[222:223]
	v_mov_b64_e32 v[58:59], v[208:209]
	v_mov_b64_e32 v[60:61], v[210:211]
	v_mov_b64_e32 v[62:63], v[216:217]
	v_mov_b64_e32 v[64:65], v[218:219]
	v_mov_b64_e32 v[66:67], v[220:221]
	v_mov_b64_e32 v[68:69], v[222:223]
	v_mov_b64_e32 v[70:71], v[216:217]
	v_mov_b64_e32 v[72:73], v[218:219]
	v_mov_b64_e32 v[74:75], v[212:213]
	v_mov_b64_e32 v[76:77], v[214:215]
	v_mov_b64_e32 v[78:79], v[208:209]
	v_mov_b64_e32 v[80:81], v[210:211]
	v_mov_b64_e32 v[82:83], v[220:221]
	v_mov_b64_e32 v[84:85], v[222:223]
	v_mov_b64_e32 v[86:87], v[216:217]
	v_mov_b64_e32 v[88:89], v[218:219]
	v_mov_b64_e32 v[90:91], v[212:213]
	v_mov_b64_e32 v[92:93], v[214:215]
	v_mov_b64_e32 v[94:95], v[208:209]
	v_mov_b64_e32 v[96:97], v[210:211]
	v_mov_b64_e32 v[98:99], v[220:221]
	v_mov_b64_e32 v[100:101], v[222:223]
	v_mov_b64_e32 v[102:103], v[216:217]
	v_mov_b64_e32 v[104:105], v[218:219]
	v_mov_b64_e32 v[106:107], v[212:213]
	v_mov_b64_e32 v[108:109], v[214:215]
	v_mov_b64_e32 v[110:111], v[208:209]
	v_mov_b64_e32 v[112:113], v[210:211]
	v_mov_b64_e32 v[114:115], v[220:221]
	v_mov_b64_e32 v[116:117], v[222:223]
	v_mov_b64_e32 v[118:119], v[216:217]
	v_mov_b64_e32 v[120:121], v[218:219]
	v_mov_b64_e32 v[122:123], v[212:213]
	v_mov_b64_e32 v[124:125], v[214:215]
	v_mov_b64_e32 v[126:127], v[208:209]
	v_mov_b64_e32 v[128:129], v[210:211]
	v_mov_b64_e32 v[130:131], v[220:221]
	v_mov_b64_e32 v[132:133], v[222:223]
	v_mov_b64_e32 v[134:135], v[216:217]
	v_mov_b64_e32 v[136:137], v[218:219]
	v_mov_b64_e32 v[138:139], v[212:213]
	v_mov_b64_e32 v[140:141], v[214:215]
	v_mov_b64_e32 v[142:143], v[208:209]
	v_mov_b64_e32 v[144:145], v[210:211]
	v_mov_b64_e32 v[146:147], v[220:221]
	v_mov_b64_e32 v[148:149], v[222:223]
	v_mov_b64_e32 v[150:151], v[216:217]
	v_mov_b64_e32 v[152:153], v[218:219]
	v_mov_b64_e32 v[154:155], v[212:213]
	v_mov_b64_e32 v[156:157], v[214:215]
	v_mov_b64_e32 v[158:159], v[208:209]
	v_mov_b64_e32 v[160:161], v[210:211]
